# P1: 72 converter workgroups (184 run the in-projection GEMM) instead of 64/192
# speedup vs baseline: 1.0215x; 1.0137x over previous
; #define LAS __attribute__((address_space(3)))
; __device__ __forceinline__ void conv_rest(Frame& F, const Args& a, int gw, int NGW) {
;     LAS unsigned* scr = (LAS unsigned*)(F.lds + F.wave * 13824);
;     bf16_t* Wpa = (bf16_t*)(F.ws + WS_WPA); bf16_t* Wpr = (bf16_t*)(F.ws + WS_WPR); bf16_t* Wout = (bf16_t*)(F.ws + WS_WOUT);
;     unsigned char* Wgu = (unsigned char*)(F.ws + WS_WGU); unsigned char* Wdn = (unsigned char*)(F.ws + WS_WDN);
;     constexpr int I_PA = (GW / 64) * (D / 32), I_PR = (D / 64) * (D / 32), I_OUT = I_PR, I_GU1 = (D / 128) * (4096 / 32), I_DN1 = (DFF / 128) * (D / 32);
;     constexpr int NITEMS = I_PA + I_PR + I_OUT;
;     for (int it = gw; it < NITEMS; it += NGW) {
;         int r = it;
;         if (r < I_PA) { transpose_item(a.in[7], GW, D, Wpa, CM_STD, r, scr, F.lane); continue; } r -= I_PA;
; __global__ void __launch_bounds__(NTHREADS, 2) mk_fwd(Args args) {
;     ...
;         const int nconv = (MK_NCONV * F.G) / 256, ngemm = F.G - nconv;
;         if ((int)blockIdx.x < ngemm) {
;             pg8::DenseSched S; S.init((const bf16_t*)(F.ws + WS_H), D, (const bf16_t*)(F.ws + WS_WIN), D, T, INW, ngemm, (int)blockIdx.x);
;             EpiInProj E{F.ws};
;             if (MK_RSYNC) pg8::gemm_phase<0, EpiInProj, pg8::DenseSched, 127, 127, true>(F.lds, S, E, &bar); else pg8::gemm_phase<0>(F.lds, S, E);
;         } else if (!MK_CONV_IN_P0) conv_rest(F, args, ((int)blockIdx.x - ngemm) * NWAVES + F.wave, nconv * NWAVES);
.LBB0_102:
	s_cmp_lt_i32 s88, 2
	s_cselect_b64 s[4:5], -1, 0
	s_and_b64 s[14:15], s[4:5], s[0:1]
	s_andn2_b64 vcc, exec, s[14:15]
	s_cbranch_vccnz .LBB0_282
	s_ashr_i32 s0, s2, 31
	s_lshr_b32 s0, s0, 30
	s_add_i32 s0, s2, s0
	s_movk_i32 s18, 72
	s_waitcnt vmcnt(6)
	v_mov_b32_e32 v18, v0
	s_sub_i32 s3, s2, s18
	s_cmp_ge_i32 s92, s3
	v_readfirstlane_b32 s4, v18
	s_mov_b64 s[0:1], -1
	s_cbranch_scc0 .LBB0_126
	s_sub_i32 s0, s92, s3
	s_ashr_i32 s19, s4, 6
	s_lshl_b32 s0, s0, 3
	s_add_i32 s21, s19, s0
	s_mul_i32 s0, s19, 0x3600
	s_add_i32 s34, s0, 0
	s_load_dwordx2 s[8:9], s[96:97], 0x68
	s_load_dwordx2 s[0:1], s[96:97], 0x78
	s_waitcnt vmcnt(4)
	v_and_b32_e32 v2, 7, v18
	v_bfe_u32 v1, v18, 3, 3
	v_lshlrev_b32_e32 v164, 4, v2
	s_lshl_b32 s20, s18, 3
	v_lshl_add_u32 v3, v1, 2, s34
	v_mul_u32_u24_e32 v4, 0x210, v2
	v_mul_u32_u24_e32 v5, 0x84, v1
	s_waitcnt vmcnt(2)
	v_add_u32_e32 v6, s34, v164
	v_and_b32_e32 v19, 63, v18
	s_mov_b32 s11, 0
	v_or_b32_e32 v173, 8, v1
	v_or_b32_e32 v168, 16, v1
	v_or_b32_e32 v169, 24, v1
	v_and_b32_e32 v174, 4, v18
	s_cmpk_gt_i32 s21, 0x13ff
	v_add_u32_e32 v170, v3, v4
	v_add_u32_e32 v171, v6, v5
	s_cbranch_scc1 .LBB0_115
	v_mov_b32_e32 v3, 0
	s_load_dwordx4 s[4:7], s[96:97], 0x38
	s_load_dwordx2 s[12:13], s[96:97], 0x48
	v_mov_b32_e32 v165, v3
	v_lshl_add_u64 v[8:9], s[94:95], 0, v[164:165]
	s_mov_b64 s[16:17], 0x3e00000
	v_lshl_add_u64 v[4:5], v[8:9], 0, s[16:17]
	s_mov_b64 s[16:17], 0x3600000
	v_lshlrev_b32_e32 v20, 2, v2
	v_lshlrev_b32_e32 v2, 3, v2
	v_lshl_add_u64 v[6:7], v[8:9], 0, s[16:17]
	s_mov_b64 s[16:17], 0x3200000
	v_lshlrev_b32_e32 v21, 14, v1
	v_and_or_b32 v22, v2, 24, v174
	v_lshlrev_b32_e32 v23, 1, v1
	v_lshl_add_u64 v[8:9], v[8:9], 0, s[16:17]
	v_lshl_or_b32 v24, s21, 6, v2
	s_lshl_b32 s22, s20, 6
	s_lshl_b32 s23, s21, 5
	s_lshl_b32 s24, s20, 5
	s_movk_i32 s25, 0x2000
	s_mov_b32 s26, 0x20000
	s_mov_b32 s27, 0x22000
	s_mov_b32 s28, 0x40000
	s_mov_b32 s29, 0x42000
	s_mov_b32 s30, 0x60000
	s_mov_b32 s31, 0x62000
	v_add_u32_e32 v25, 0x420, v171
	v_add_u32_e32 v26, 0x428, v171
	v_add_u32_e32 v27, 0x840, v171
	v_add_u32_e32 v28, 0x848, v171
	v_add_u32_e32 v29, 0xc60, v171
	s_waitcnt vmcnt(1)
	v_add_u32_e32 v30, 0xc68, v171
	s_mov_b32 s33, s21
	s_branch .LBB0_107
